# P0 conditioning-vector fill: 32 loads issued together then silu + LDS writes (was one dependent load per iteration); T1 counted vmcnt
# speedup vs baseline: 1.0077x; 1.0077x over previous
; __device__ __forceinline__ float silu_f(float x) { return x / (1.f + __expf(-x)); }
; __device__ __forceinline__ void p0_ada(Frame& F, const float* c, const float* ada_w, const float* ada_b, float* mod) {
;     ...
;     for (int i = F.tid; i < NB * D; i += NTHR) { const int b = i / D, k = i % D; cond[k * 8 + b] = silu_f(c[i]); }
;     __syncthreads();
.LBB0_15:
	v_lshlrev_b32_e32 v14, 5, v0
	global_load_dword v20, v[4:5], off
	v_lshl_add_u64 v[4:5], v[4:5], 0, s[8:9]
	global_load_dword v21, v[4:5], off
	v_lshl_add_u64 v[4:5], v[4:5], 0, s[8:9]
	global_load_dword v22, v[4:5], off
	v_lshl_add_u64 v[4:5], v[4:5], 0, s[8:9]
	global_load_dword v23, v[4:5], off
	v_lshl_add_u64 v[4:5], v[4:5], 0, s[8:9]
	global_load_dword v24, v[4:5], off
	v_lshl_add_u64 v[4:5], v[4:5], 0, s[8:9]
	global_load_dword v25, v[4:5], off
	v_lshl_add_u64 v[4:5], v[4:5], 0, s[8:9]
	global_load_dword v26, v[4:5], off
	v_lshl_add_u64 v[4:5], v[4:5], 0, s[8:9]
	global_load_dword v27, v[4:5], off
	v_lshl_add_u64 v[4:5], v[4:5], 0, s[8:9]
	global_load_dword v28, v[4:5], off
	v_lshl_add_u64 v[4:5], v[4:5], 0, s[8:9]
	global_load_dword v29, v[4:5], off
	v_lshl_add_u64 v[4:5], v[4:5], 0, s[8:9]
	global_load_dword v30, v[4:5], off
	v_lshl_add_u64 v[4:5], v[4:5], 0, s[8:9]
	global_load_dword v31, v[4:5], off
	v_lshl_add_u64 v[4:5], v[4:5], 0, s[8:9]
	global_load_dword v32, v[4:5], off
	v_lshl_add_u64 v[4:5], v[4:5], 0, s[8:9]
	global_load_dword v33, v[4:5], off
	v_lshl_add_u64 v[4:5], v[4:5], 0, s[8:9]
	global_load_dword v34, v[4:5], off
	v_lshl_add_u64 v[4:5], v[4:5], 0, s[8:9]
	global_load_dword v35, v[4:5], off
	v_lshl_add_u64 v[4:5], v[4:5], 0, s[8:9]
	global_load_dword v36, v[4:5], off
	v_lshl_add_u64 v[4:5], v[4:5], 0, s[8:9]
	global_load_dword v37, v[4:5], off
	v_lshl_add_u64 v[4:5], v[4:5], 0, s[8:9]
	global_load_dword v38, v[4:5], off
	v_lshl_add_u64 v[4:5], v[4:5], 0, s[8:9]
	global_load_dword v39, v[4:5], off
	v_lshl_add_u64 v[4:5], v[4:5], 0, s[8:9]
	global_load_dword v40, v[4:5], off
	v_lshl_add_u64 v[4:5], v[4:5], 0, s[8:9]
	global_load_dword v41, v[4:5], off
	v_lshl_add_u64 v[4:5], v[4:5], 0, s[8:9]
	global_load_dword v42, v[4:5], off
	v_lshl_add_u64 v[4:5], v[4:5], 0, s[8:9]
	global_load_dword v43, v[4:5], off
	v_lshl_add_u64 v[4:5], v[4:5], 0, s[8:9]
	global_load_dword v44, v[4:5], off
	v_lshl_add_u64 v[4:5], v[4:5], 0, s[8:9]
	global_load_dword v45, v[4:5], off
	v_lshl_add_u64 v[4:5], v[4:5], 0, s[8:9]
	global_load_dword v46, v[4:5], off
	v_lshl_add_u64 v[4:5], v[4:5], 0, s[8:9]
	global_load_dword v47, v[4:5], off
	v_lshl_add_u64 v[4:5], v[4:5], 0, s[8:9]
	global_load_dword v48, v[4:5], off
	v_lshl_add_u64 v[4:5], v[4:5], 0, s[8:9]
	global_load_dword v49, v[4:5], off
	v_lshl_add_u64 v[4:5], v[4:5], 0, s[8:9]
	global_load_dword v50, v[4:5], off
	v_lshl_add_u64 v[4:5], v[4:5], 0, s[8:9]
	global_load_dword v51, v[4:5], off
	s_waitcnt vmcnt(0)
	v_mul_f32_e32 v9, 0xbfb8aa3b, v20
	v_exp_f32_e32 v9, v9
	s_nop 0
	v_add_f32_e32 v8, 1.0, v9
	v_div_scale_f32 v9, s[12:13], v8, v8, v20
	v_rcp_f32_e32 v10, v9
	v_div_scale_f32 v11, vcc, v20, v8, v20
	v_fma_f32 v12, -v9, v10, 1.0
	v_fmac_f32_e32 v10, v12, v10
	v_mul_f32_e32 v12, v11, v10
	v_fma_f32 v13, -v9, v12, v11
	v_fmac_f32_e32 v12, v13, v10
	v_fma_f32 v9, -v9, v12, v11
	v_div_fmas_f32 v9, v9, v10, v12
	v_div_fixup_f32 v6, v9, v8, v20
	ds_write_b32 v14, v6
	v_mul_f32_e32 v9, 0xbfb8aa3b, v21
	v_exp_f32_e32 v9, v9
	s_nop 0
	v_add_f32_e32 v8, 1.0, v9
	v_div_scale_f32 v9, s[12:13], v8, v8, v21
	v_rcp_f32_e32 v10, v9
	v_div_scale_f32 v11, vcc, v21, v8, v21
	v_fma_f32 v12, -v9, v10, 1.0
	v_fmac_f32_e32 v10, v12, v10
	v_mul_f32_e32 v12, v11, v10
	v_fma_f32 v13, -v9, v12, v11
	v_fmac_f32_e32 v12, v13, v10
	v_fma_f32 v9, -v9, v12, v11
	v_div_fmas_f32 v9, v9, v10, v12
	v_div_fixup_f32 v6, v9, v8, v21
	ds_write_b32 v14, v6 offset:16384
	v_mul_f32_e32 v9, 0xbfb8aa3b, v22
	v_exp_f32_e32 v9, v9
	s_nop 0
	v_add_f32_e32 v8, 1.0, v9
	v_div_scale_f32 v9, s[12:13], v8, v8, v22
	v_rcp_f32_e32 v10, v9
	v_div_scale_f32 v11, vcc, v22, v8, v22
	v_fma_f32 v12, -v9, v10, 1.0
	v_fmac_f32_e32 v10, v12, v10
	v_mul_f32_e32 v12, v11, v10
	v_fma_f32 v13, -v9, v12, v11
	v_fmac_f32_e32 v12, v13, v10
	v_fma_f32 v9, -v9, v12, v11
	v_div_fmas_f32 v9, v9, v10, v12
	v_div_fixup_f32 v6, v9, v8, v22
	ds_write_b32 v14, v6 offset:32768
	v_mul_f32_e32 v9, 0xbfb8aa3b, v23
	v_exp_f32_e32 v9, v9
	s_nop 0
	v_add_f32_e32 v8, 1.0, v9
	v_div_scale_f32 v9, s[12:13], v8, v8, v23
	v_rcp_f32_e32 v10, v9
	v_div_scale_f32 v11, vcc, v23, v8, v23
	v_fma_f32 v12, -v9, v10, 1.0
	v_fmac_f32_e32 v10, v12, v10
	v_mul_f32_e32 v12, v11, v10
	v_fma_f32 v13, -v9, v12, v11
	v_fmac_f32_e32 v12, v13, v10
	v_fma_f32 v9, -v9, v12, v11
	v_div_fmas_f32 v9, v9, v10, v12
	v_div_fixup_f32 v6, v9, v8, v23
	ds_write_b32 v14, v6 offset:49152
	v_mul_f32_e32 v9, 0xbfb8aa3b, v24
	v_exp_f32_e32 v9, v9
	s_nop 0
	v_add_f32_e32 v8, 1.0, v9
	v_div_scale_f32 v9, s[12:13], v8, v8, v24
	v_rcp_f32_e32 v10, v9
	v_div_scale_f32 v11, vcc, v24, v8, v24
	v_fma_f32 v12, -v9, v10, 1.0
	v_fmac_f32_e32 v10, v12, v10
	v_mul_f32_e32 v12, v11, v10
	v_fma_f32 v13, -v9, v12, v11
	v_fmac_f32_e32 v12, v13, v10
	v_fma_f32 v9, -v9, v12, v11
	v_div_fmas_f32 v9, v9, v10, v12
	v_div_fixup_f32 v6, v9, v8, v24
	ds_write_b32 v14, v6 offset:4
	v_mul_f32_e32 v9, 0xbfb8aa3b, v25
	v_exp_f32_e32 v9, v9
	s_nop 0
	v_add_f32_e32 v8, 1.0, v9
	v_div_scale_f32 v9, s[12:13], v8, v8, v25
	v_rcp_f32_e32 v10, v9
	v_div_scale_f32 v11, vcc, v25, v8, v25
	v_fma_f32 v12, -v9, v10, 1.0
	v_fmac_f32_e32 v10, v12, v10
	v_mul_f32_e32 v12, v11, v10
	v_fma_f32 v13, -v9, v12, v11
	v_fmac_f32_e32 v12, v13, v10
	v_fma_f32 v9, -v9, v12, v11
	v_div_fmas_f32 v9, v9, v10, v12
	v_div_fixup_f32 v6, v9, v8, v25
	ds_write_b32 v14, v6 offset:16388
	v_mul_f32_e32 v9, 0xbfb8aa3b, v26
	v_exp_f32_e32 v9, v9
	s_nop 0
	v_add_f32_e32 v8, 1.0, v9
	v_div_scale_f32 v9, s[12:13], v8, v8, v26
	v_rcp_f32_e32 v10, v9
	v_div_scale_f32 v11, vcc, v26, v8, v26
	v_fma_f32 v12, -v9, v10, 1.0
	v_fmac_f32_e32 v10, v12, v10
	v_mul_f32_e32 v12, v11, v10
; __device__ __forceinline__ float silu_f(float x) { return x / (1.f + __expf(-x)); }
; __device__ __forceinline__ void p0_ada(Frame& F, const float* c, const float* ada_w, const float* ada_b, float* mod) {
;     ...
;     for (int i = F.tid; i < NB * D; i += NTHR) { const int b = i / D, k = i % D; cond[k * 8 + b] = silu_f(c[i]); }
	v_fma_f32 v13, -v9, v12, v11
	v_fmac_f32_e32 v12, v13, v10
	v_fma_f32 v9, -v9, v12, v11
	v_div_fmas_f32 v9, v9, v10, v12
	v_div_fixup_f32 v6, v9, v8, v26
	ds_write_b32 v14, v6 offset:32772
	v_mul_f32_e32 v9, 0xbfb8aa3b, v27
	v_exp_f32_e32 v9, v9
	s_nop 0
	v_add_f32_e32 v8, 1.0, v9
	v_div_scale_f32 v9, s[12:13], v8, v8, v27
	v_rcp_f32_e32 v10, v9
	v_div_scale_f32 v11, vcc, v27, v8, v27
	v_fma_f32 v12, -v9, v10, 1.0
	v_fmac_f32_e32 v10, v12, v10
	v_mul_f32_e32 v12, v11, v10
	v_fma_f32 v13, -v9, v12, v11
	v_fmac_f32_e32 v12, v13, v10
	v_fma_f32 v9, -v9, v12, v11
	v_div_fmas_f32 v9, v9, v10, v12
	v_div_fixup_f32 v6, v9, v8, v27
	ds_write_b32 v14, v6 offset:49156
	v_mul_f32_e32 v9, 0xbfb8aa3b, v28
	v_exp_f32_e32 v9, v9
	s_nop 0
	v_add_f32_e32 v8, 1.0, v9
	v_div_scale_f32 v9, s[12:13], v8, v8, v28
	v_rcp_f32_e32 v10, v9
	v_div_scale_f32 v11, vcc, v28, v8, v28
	v_fma_f32 v12, -v9, v10, 1.0
	v_fmac_f32_e32 v10, v12, v10
	v_mul_f32_e32 v12, v11, v10
	v_fma_f32 v13, -v9, v12, v11
	v_fmac_f32_e32 v12, v13, v10
	v_fma_f32 v9, -v9, v12, v11
	v_div_fmas_f32 v9, v9, v10, v12
	v_div_fixup_f32 v6, v9, v8, v28
	ds_write_b32 v14, v6 offset:8
	v_mul_f32_e32 v9, 0xbfb8aa3b, v29
	v_exp_f32_e32 v9, v9
	s_nop 0
	v_add_f32_e32 v8, 1.0, v9
	v_div_scale_f32 v9, s[12:13], v8, v8, v29
	v_rcp_f32_e32 v10, v9
	v_div_scale_f32 v11, vcc, v29, v8, v29
	v_fma_f32 v12, -v9, v10, 1.0
	v_fmac_f32_e32 v10, v12, v10
	v_mul_f32_e32 v12, v11, v10
	v_fma_f32 v13, -v9, v12, v11
	v_fmac_f32_e32 v12, v13, v10
	v_fma_f32 v9, -v9, v12, v11
	v_div_fmas_f32 v9, v9, v10, v12
	v_div_fixup_f32 v6, v9, v8, v29
	ds_write_b32 v14, v6 offset:16392
	v_mul_f32_e32 v9, 0xbfb8aa3b, v30
	v_exp_f32_e32 v9, v9
	s_nop 0
	v_add_f32_e32 v8, 1.0, v9
	v_div_scale_f32 v9, s[12:13], v8, v8, v30
	v_rcp_f32_e32 v10, v9
	v_div_scale_f32 v11, vcc, v30, v8, v30
	v_fma_f32 v12, -v9, v10, 1.0
	v_fmac_f32_e32 v10, v12, v10
	v_mul_f32_e32 v12, v11, v10
	v_fma_f32 v13, -v9, v12, v11
	v_fmac_f32_e32 v12, v13, v10
	v_fma_f32 v9, -v9, v12, v11
	v_div_fmas_f32 v9, v9, v10, v12
	v_div_fixup_f32 v6, v9, v8, v30
	ds_write_b32 v14, v6 offset:32776
	v_mul_f32_e32 v9, 0xbfb8aa3b, v31
	v_exp_f32_e32 v9, v9
	s_nop 0
	v_add_f32_e32 v8, 1.0, v9
	v_div_scale_f32 v9, s[12:13], v8, v8, v31
	v_rcp_f32_e32 v10, v9
	v_div_scale_f32 v11, vcc, v31, v8, v31
	v_fma_f32 v12, -v9, v10, 1.0
	v_fmac_f32_e32 v10, v12, v10
	v_mul_f32_e32 v12, v11, v10
	v_fma_f32 v13, -v9, v12, v11
	v_fmac_f32_e32 v12, v13, v10
	v_fma_f32 v9, -v9, v12, v11
	v_div_fmas_f32 v9, v9, v10, v12
	v_div_fixup_f32 v6, v9, v8, v31
	ds_write_b32 v14, v6 offset:49160
	v_mul_f32_e32 v9, 0xbfb8aa3b, v32
	v_exp_f32_e32 v9, v9
	s_nop 0
	v_add_f32_e32 v8, 1.0, v9
	v_div_scale_f32 v9, s[12:13], v8, v8, v32
	v_rcp_f32_e32 v10, v9
	v_div_scale_f32 v11, vcc, v32, v8, v32
	v_fma_f32 v12, -v9, v10, 1.0
	v_fmac_f32_e32 v10, v12, v10
	v_mul_f32_e32 v12, v11, v10
	v_fma_f32 v13, -v9, v12, v11
	v_fmac_f32_e32 v12, v13, v10
	v_fma_f32 v9, -v9, v12, v11
	v_div_fmas_f32 v9, v9, v10, v12
	v_div_fixup_f32 v6, v9, v8, v32
	ds_write_b32 v14, v6 offset:12
	v_mul_f32_e32 v9, 0xbfb8aa3b, v33
	v_exp_f32_e32 v9, v9
	s_nop 0
	v_add_f32_e32 v8, 1.0, v9
	v_div_scale_f32 v9, s[12:13], v8, v8, v33
	v_rcp_f32_e32 v10, v9
	v_div_scale_f32 v11, vcc, v33, v8, v33
	v_fma_f32 v12, -v9, v10, 1.0
	v_fmac_f32_e32 v10, v12, v10
	v_mul_f32_e32 v12, v11, v10
	v_fma_f32 v13, -v9, v12, v11
	v_fmac_f32_e32 v12, v13, v10
	v_fma_f32 v9, -v9, v12, v11
	v_div_fmas_f32 v9, v9, v10, v12
	v_div_fixup_f32 v6, v9, v8, v33
	ds_write_b32 v14, v6 offset:16396
	v_mul_f32_e32 v9, 0xbfb8aa3b, v34
	v_exp_f32_e32 v9, v9
	s_nop 0
	v_add_f32_e32 v8, 1.0, v9
	v_div_scale_f32 v9, s[12:13], v8, v8, v34
	v_rcp_f32_e32 v10, v9
	v_div_scale_f32 v11, vcc, v34, v8, v34
	v_fma_f32 v12, -v9, v10, 1.0
	v_fmac_f32_e32 v10, v12, v10
	v_mul_f32_e32 v12, v11, v10
	v_fma_f32 v13, -v9, v12, v11
	v_fmac_f32_e32 v12, v13, v10
	v_fma_f32 v9, -v9, v12, v11
	v_div_fmas_f32 v9, v9, v10, v12
	v_div_fixup_f32 v6, v9, v8, v34
	ds_write_b32 v14, v6 offset:32780
	v_mul_f32_e32 v9, 0xbfb8aa3b, v35
	v_exp_f32_e32 v9, v9
	s_nop 0
	v_add_f32_e32 v8, 1.0, v9
	v_div_scale_f32 v9, s[12:13], v8, v8, v35
	v_rcp_f32_e32 v10, v9
	v_div_scale_f32 v11, vcc, v35, v8, v35
	v_fma_f32 v12, -v9, v10, 1.0
	v_fmac_f32_e32 v10, v12, v10
	v_mul_f32_e32 v12, v11, v10
	v_fma_f32 v13, -v9, v12, v11
	v_fmac_f32_e32 v12, v13, v10
	v_fma_f32 v9, -v9, v12, v11
	v_div_fmas_f32 v9, v9, v10, v12
	v_div_fixup_f32 v6, v9, v8, v35
	ds_write_b32 v14, v6 offset:49164
	v_mul_f32_e32 v9, 0xbfb8aa3b, v36
	v_exp_f32_e32 v9, v9
	s_nop 0
	v_add_f32_e32 v8, 1.0, v9
	v_div_scale_f32 v9, s[12:13], v8, v8, v36
	v_rcp_f32_e32 v10, v9
	v_div_scale_f32 v11, vcc, v36, v8, v36
	v_fma_f32 v12, -v9, v10, 1.0
	v_fmac_f32_e32 v10, v12, v10
	v_mul_f32_e32 v12, v11, v10
	v_fma_f32 v13, -v9, v12, v11
	v_fmac_f32_e32 v12, v13, v10
	v_fma_f32 v9, -v9, v12, v11
	v_div_fmas_f32 v9, v9, v10, v12
	v_div_fixup_f32 v6, v9, v8, v36
	ds_write_b32 v14, v6 offset:16
	v_mul_f32_e32 v9, 0xbfb8aa3b, v37
	v_exp_f32_e32 v9, v9
	s_nop 0
	v_add_f32_e32 v8, 1.0, v9
	v_div_scale_f32 v9, s[12:13], v8, v8, v37
	v_rcp_f32_e32 v10, v9
	v_div_scale_f32 v11, vcc, v37, v8, v37
	v_fma_f32 v12, -v9, v10, 1.0
	v_fmac_f32_e32 v10, v12, v10
	v_mul_f32_e32 v12, v11, v10
	v_fma_f32 v13, -v9, v12, v11
	v_fmac_f32_e32 v12, v13, v10
	v_fma_f32 v9, -v9, v12, v11
	v_div_fmas_f32 v9, v9, v10, v12
	v_div_fixup_f32 v6, v9, v8, v37
	ds_write_b32 v14, v6 offset:16400
	v_mul_f32_e32 v9, 0xbfb8aa3b, v38
	v_exp_f32_e32 v9, v9
	s_nop 0
	v_add_f32_e32 v8, 1.0, v9
	v_div_scale_f32 v9, s[12:13], v8, v8, v38
	v_rcp_f32_e32 v10, v9
	v_div_scale_f32 v11, vcc, v38, v8, v38
; __device__ __forceinline__ float silu_f(float x) { return x / (1.f + __expf(-x)); }
; __device__ __forceinline__ void p0_ada(Frame& F, const float* c, const float* ada_w, const float* ada_b, float* mod) {
;     ...
;     for (int i = F.tid; i < NB * D; i += NTHR) { const int b = i / D, k = i % D; cond[k * 8 + b] = silu_f(c[i]); }
;     __syncthreads();
	v_fma_f32 v12, -v9, v10, 1.0
	v_fmac_f32_e32 v10, v12, v10
	v_mul_f32_e32 v12, v11, v10
	v_fma_f32 v13, -v9, v12, v11
	v_fmac_f32_e32 v12, v13, v10
	v_fma_f32 v9, -v9, v12, v11
	v_div_fmas_f32 v9, v9, v10, v12
	v_div_fixup_f32 v6, v9, v8, v38
	ds_write_b32 v14, v6 offset:32784
	v_mul_f32_e32 v9, 0xbfb8aa3b, v39
	v_exp_f32_e32 v9, v9
	s_nop 0
	v_add_f32_e32 v8, 1.0, v9
	v_div_scale_f32 v9, s[12:13], v8, v8, v39
	v_rcp_f32_e32 v10, v9
	v_div_scale_f32 v11, vcc, v39, v8, v39
	v_fma_f32 v12, -v9, v10, 1.0
	v_fmac_f32_e32 v10, v12, v10
	v_mul_f32_e32 v12, v11, v10
	v_fma_f32 v13, -v9, v12, v11
	v_fmac_f32_e32 v12, v13, v10
	v_fma_f32 v9, -v9, v12, v11
	v_div_fmas_f32 v9, v9, v10, v12
	v_div_fixup_f32 v6, v9, v8, v39
	ds_write_b32 v14, v6 offset:49168
	v_mul_f32_e32 v9, 0xbfb8aa3b, v40
	v_exp_f32_e32 v9, v9
	s_nop 0
	v_add_f32_e32 v8, 1.0, v9
	v_div_scale_f32 v9, s[12:13], v8, v8, v40
	v_rcp_f32_e32 v10, v9
	v_div_scale_f32 v11, vcc, v40, v8, v40
	v_fma_f32 v12, -v9, v10, 1.0
	v_fmac_f32_e32 v10, v12, v10
	v_mul_f32_e32 v12, v11, v10
	v_fma_f32 v13, -v9, v12, v11
	v_fmac_f32_e32 v12, v13, v10
	v_fma_f32 v9, -v9, v12, v11
	v_div_fmas_f32 v9, v9, v10, v12
	v_div_fixup_f32 v6, v9, v8, v40
	ds_write_b32 v14, v6 offset:20
	v_mul_f32_e32 v9, 0xbfb8aa3b, v41
	v_exp_f32_e32 v9, v9
	s_nop 0
	v_add_f32_e32 v8, 1.0, v9
	v_div_scale_f32 v9, s[12:13], v8, v8, v41
	v_rcp_f32_e32 v10, v9
	v_div_scale_f32 v11, vcc, v41, v8, v41
	v_fma_f32 v12, -v9, v10, 1.0
	v_fmac_f32_e32 v10, v12, v10
	v_mul_f32_e32 v12, v11, v10
	v_fma_f32 v13, -v9, v12, v11
	v_fmac_f32_e32 v12, v13, v10
	v_fma_f32 v9, -v9, v12, v11
	v_div_fmas_f32 v9, v9, v10, v12
	v_div_fixup_f32 v6, v9, v8, v41
	ds_write_b32 v14, v6 offset:16404
	v_mul_f32_e32 v9, 0xbfb8aa3b, v42
	v_exp_f32_e32 v9, v9
	s_nop 0
	v_add_f32_e32 v8, 1.0, v9
	v_div_scale_f32 v9, s[12:13], v8, v8, v42
	v_rcp_f32_e32 v10, v9
	v_div_scale_f32 v11, vcc, v42, v8, v42
	v_fma_f32 v12, -v9, v10, 1.0
	v_fmac_f32_e32 v10, v12, v10
	v_mul_f32_e32 v12, v11, v10
	v_fma_f32 v13, -v9, v12, v11
	v_fmac_f32_e32 v12, v13, v10
	v_fma_f32 v9, -v9, v12, v11
	v_div_fmas_f32 v9, v9, v10, v12
	v_div_fixup_f32 v6, v9, v8, v42
	ds_write_b32 v14, v6 offset:32788
	v_mul_f32_e32 v9, 0xbfb8aa3b, v43
	v_exp_f32_e32 v9, v9
	s_nop 0
	v_add_f32_e32 v8, 1.0, v9
	v_div_scale_f32 v9, s[12:13], v8, v8, v43
	v_rcp_f32_e32 v10, v9
	v_div_scale_f32 v11, vcc, v43, v8, v43
	v_fma_f32 v12, -v9, v10, 1.0
	v_fmac_f32_e32 v10, v12, v10
	v_mul_f32_e32 v12, v11, v10
	v_fma_f32 v13, -v9, v12, v11
	v_fmac_f32_e32 v12, v13, v10
	v_fma_f32 v9, -v9, v12, v11
	v_div_fmas_f32 v9, v9, v10, v12
	v_div_fixup_f32 v6, v9, v8, v43
	ds_write_b32 v14, v6 offset:49172
	v_mul_f32_e32 v9, 0xbfb8aa3b, v44
	v_exp_f32_e32 v9, v9
	s_nop 0
	v_add_f32_e32 v8, 1.0, v9
	v_div_scale_f32 v9, s[12:13], v8, v8, v44
	v_rcp_f32_e32 v10, v9
	v_div_scale_f32 v11, vcc, v44, v8, v44
	v_fma_f32 v12, -v9, v10, 1.0
	v_fmac_f32_e32 v10, v12, v10
	v_mul_f32_e32 v12, v11, v10
	v_fma_f32 v13, -v9, v12, v11
	v_fmac_f32_e32 v12, v13, v10
	v_fma_f32 v9, -v9, v12, v11
	v_div_fmas_f32 v9, v9, v10, v12
	v_div_fixup_f32 v6, v9, v8, v44
	ds_write_b32 v14, v6 offset:24
	v_mul_f32_e32 v9, 0xbfb8aa3b, v45
	v_exp_f32_e32 v9, v9
	s_nop 0
	v_add_f32_e32 v8, 1.0, v9
	v_div_scale_f32 v9, s[12:13], v8, v8, v45
	v_rcp_f32_e32 v10, v9
	v_div_scale_f32 v11, vcc, v45, v8, v45
	v_fma_f32 v12, -v9, v10, 1.0
	v_fmac_f32_e32 v10, v12, v10
	v_mul_f32_e32 v12, v11, v10
	v_fma_f32 v13, -v9, v12, v11
	v_fmac_f32_e32 v12, v13, v10
	v_fma_f32 v9, -v9, v12, v11
	v_div_fmas_f32 v9, v9, v10, v12
	v_div_fixup_f32 v6, v9, v8, v45
	ds_write_b32 v14, v6 offset:16408
	v_mul_f32_e32 v9, 0xbfb8aa3b, v46
	v_exp_f32_e32 v9, v9
	s_nop 0
	v_add_f32_e32 v8, 1.0, v9
	v_div_scale_f32 v9, s[12:13], v8, v8, v46
	v_rcp_f32_e32 v10, v9
	v_div_scale_f32 v11, vcc, v46, v8, v46
	v_fma_f32 v12, -v9, v10, 1.0
	v_fmac_f32_e32 v10, v12, v10
	v_mul_f32_e32 v12, v11, v10
	v_fma_f32 v13, -v9, v12, v11
	v_fmac_f32_e32 v12, v13, v10
	v_fma_f32 v9, -v9, v12, v11
	v_div_fmas_f32 v9, v9, v10, v12
	v_div_fixup_f32 v6, v9, v8, v46
	ds_write_b32 v14, v6 offset:32792
	v_mul_f32_e32 v9, 0xbfb8aa3b, v47
	v_exp_f32_e32 v9, v9
	s_nop 0
	v_add_f32_e32 v8, 1.0, v9
	v_div_scale_f32 v9, s[12:13], v8, v8, v47
	v_rcp_f32_e32 v10, v9
	v_div_scale_f32 v11, vcc, v47, v8, v47
	v_fma_f32 v12, -v9, v10, 1.0
	v_fmac_f32_e32 v10, v12, v10
	v_mul_f32_e32 v12, v11, v10
	v_fma_f32 v13, -v9, v12, v11
	v_fmac_f32_e32 v12, v13, v10
	v_fma_f32 v9, -v9, v12, v11
	v_div_fmas_f32 v9, v9, v10, v12
	v_div_fixup_f32 v6, v9, v8, v47
	ds_write_b32 v14, v6 offset:49176
	v_mul_f32_e32 v9, 0xbfb8aa3b, v48
	v_exp_f32_e32 v9, v9
	s_nop 0
	v_add_f32_e32 v8, 1.0, v9
	v_div_scale_f32 v9, s[12:13], v8, v8, v48
	v_rcp_f32_e32 v10, v9
	v_div_scale_f32 v11, vcc, v48, v8, v48
	v_fma_f32 v12, -v9, v10, 1.0
	v_fmac_f32_e32 v10, v12, v10
	v_mul_f32_e32 v12, v11, v10
	v_fma_f32 v13, -v9, v12, v11
	v_fmac_f32_e32 v12, v13, v10
	v_fma_f32 v9, -v9, v12, v11
	v_div_fmas_f32 v9, v9, v10, v12
	v_div_fixup_f32 v6, v9, v8, v48
	ds_write_b32 v14, v6 offset:28
	v_mul_f32_e32 v9, 0xbfb8aa3b, v49
	v_exp_f32_e32 v9, v9
	s_nop 0
	v_add_f32_e32 v8, 1.0, v9
	v_div_scale_f32 v9, s[12:13], v8, v8, v49
	v_rcp_f32_e32 v10, v9
	v_div_scale_f32 v11, vcc, v49, v8, v49
	v_fma_f32 v12, -v9, v10, 1.0
	v_fmac_f32_e32 v10, v12, v10
	v_mul_f32_e32 v12, v11, v10
	v_fma_f32 v13, -v9, v12, v11
	v_fmac_f32_e32 v12, v13, v10
	v_fma_f32 v9, -v9, v12, v11
	v_div_fmas_f32 v9, v9, v10, v12
	v_div_fixup_f32 v6, v9, v8, v49
	ds_write_b32 v14, v6 offset:16412
	v_mul_f32_e32 v9, 0xbfb8aa3b, v50
	v_exp_f32_e32 v9, v9
	s_nop 0
	v_add_f32_e32 v8, 1.0, v9
	v_div_scale_f32 v9, s[12:13], v8, v8, v50
	v_rcp_f32_e32 v10, v9
	v_div_scale_f32 v11, vcc, v50, v8, v50
	v_fma_f32 v12, -v9, v10, 1.0
	v_fmac_f32_e32 v10, v12, v10
	v_mul_f32_e32 v12, v11, v10
	v_fma_f32 v13, -v9, v12, v11
	v_fmac_f32_e32 v12, v13, v10
	v_fma_f32 v9, -v9, v12, v11
	v_div_fmas_f32 v9, v9, v10, v12
	v_div_fixup_f32 v6, v9, v8, v50
	ds_write_b32 v14, v6 offset:32796
	v_mul_f32_e32 v9, 0xbfb8aa3b, v51
	v_exp_f32_e32 v9, v9
	s_nop 0
	v_add_f32_e32 v8, 1.0, v9
	v_div_scale_f32 v9, s[12:13], v8, v8, v51
	v_rcp_f32_e32 v10, v9
	v_div_scale_f32 v11, vcc, v51, v8, v51
	v_fma_f32 v12, -v9, v10, 1.0
	v_fmac_f32_e32 v10, v12, v10
	v_mul_f32_e32 v12, v11, v10
	v_fma_f32 v13, -v9, v12, v11
	v_fmac_f32_e32 v12, v13, v10
	v_fma_f32 v9, -v9, v12, v11
	v_div_fmas_f32 v9, v9, v10, v12
	v_div_fixup_f32 v6, v9, v8, v51
	ds_write_b32 v14, v6 offset:49180
	s_cmpk_gt_i32 s2, 0x2ff
	v_lshrrev_b32_e32 v72, 3, v194
	s_waitcnt lgkmcnt(0)
	s_barrier
; __device__ __forceinline__ void p0_ada(Frame& F, const float* c, const float* ada_w, const float* ada_b, float* mod) {
;     ...
;     const int cq = F.lane & 7, ks = F.lane >> 3;
;     for (int u = blockIdx.x; u < 768; u += F.G) {
;         const int l = u / 384, cb = u % 384;
;         const float* W = ada_w + (size_t)l * D * 6 * D + cb * 32 + cq * 4;
;         f32x4 acc[8];
; #pragma unroll
;         for (int b = 0; b < 8; ++b) acc[b] = (f32x4){0.f, 0.f, 0.f, 0.f};
;         const int kbase = F.wave * 256 + ks;
; #pragma unroll 4
;         for (int it = 0; it < 32; ++it) {
;             const int k = kbase + 8 * it;
;             const f32x4 w = __builtin_nontemporal_load((const f32x4*)(W + (size_t)k * 6 * D));
;             const f32x4 c0 = *(const f32x4*)(cond + k * 8), c1 = *(const f32x4*)(cond + k * 8 + 4);
;             acc[0] += w * c0[0]; acc[1] += w * c0[1]; acc[2] += w * c0[2]; acc[3] += w * c0[3];
;             acc[4] += w * c1[0]; acc[5] += w * c1[1]; acc[6] += w * c1[2]; acc[7] += w * c1[3];
;         }
; #pragma unroll
;         for (int b = 0; b < 8; ++b)
; #pragma unroll
;             for (int j = 0; j < 4; ++j) { float v = acc[b][j]; v += __shfl_xor(v, 8); v += __shfl_xor(v, 16); v += __shfl_xor(v, 32); acc[b][j] = v; }
;         if (F.lane < 8) {
; #pragma unroll
;             for (int b = 0; b < 8; ++b) *(f32x4*)(part + (F.wave * 8 + b) * 32 + cq * 4) = acc[b];
;         }
;         __syncthreads();
;         if (F.tid < 256) { const int b = F.tid >> 5, col = F.tid & 31; float s = ada_b[(size_t)l * 6 * D + cb * 32 + col];
	s_cbranch_scc1 .LBB0_25
	v_mbcnt_lo_u32_b32 v1, -1, 0
	v_mbcnt_hi_u32_b32 v3, -1, v1
	v_and_b32_e32 v5, 64, v3
	v_xor_b32_e32 v1, 8, v3
	v_add_u32_e32 v5, 64, v5
	v_cmp_lt_i32_e32 vcc, v1, v5
	v_xor_b32_e32 v6, 16, v3
	s_add_u32 s8, s50, 0x100000
	v_cndmask_b32_e32 v1, v3, v1, vcc
	v_cmp_lt_i32_e32 vcc, v6, v5
	v_readlane_b32 s12, v255, 9
	s_addc_u32 s9, s51, 0
	v_cndmask_b32_e32 v6, v3, v6, vcc
	v_lshlrev_b32_e32 v13, 2, v6
	v_xor_b32_e32 v6, 32, v3
	s_add_i32 s10, 0, 0x10000
	s_lshl_b32 s11, s12, 10
	v_cmp_lt_i32_e32 vcc, v6, v5
	s_add_i32 s11, s11, s10
	v_add_u32_e32 v75, s10, v2
	s_lshl_b32 s10, s12, 13
	v_and_b32_e32 v4, 28, v2
	v_mov_b32_e32 v11, 0
	v_cndmask_b32_e32 v3, v3, v6, vcc
	s_movk_i32 s6, 0x100
	v_and_b32_e32 v6, 31, v0
	s_add_i32 s10, s10, 0
	v_lshlrev_b32_e32 v1, 2, v1
	v_lshlrev_b32_e32 v73, 2, v3
	v_cmp_gt_u32_e32 vcc, 8, v194
	v_cmp_gt_u32_e64 s[6:7], s6, v0
	v_lshl_add_u32 v74, v4, 2, s11
	v_lshrrev_b32_e32 v12, 5, v0
	v_lshl_add_u32 v76, v72, 5, s10
	v_lshl_or_b32 v77, s12, 8, v72
	v_lshlrev_b32_e32 v14, 2, v4
	v_mov_b32_e32 v15, v11
	s_mov_b32 s15, 0xc000
	v_lshlrev_b32_e32 v10, 2, v6
	s_mov_b32 s16, s2
	s_branch .LBB0_19
